# PEER query projection (P6 GEMM output) kept in MFMA-fragment order in place: epilogue stores and P7 query fragment loads become lane-contiguous
# speedup vs baseline: 1.0387x; 1.0041x over previous
; __device__ __forceinline__ unsigned cvt_pk_bf16(float lo, float hi) { unsigned r; asm volatile("v_cvt_pk_bf16_f32 %0, %1, %2" : "=v"(r) : "v"(lo), "v"(hi)); return r; }
;     __device__ __forceinline__ void operator()(const f32x4 (&acc)[2][2][4][2], const Unit& u, int wr, int wc, int fr, int fq) const {
;         const int row0 = u.pm * BM + wr * 64 + fr, col0 = u.pn * BM + wc * 32 + 8 * fq;
; #pragma unroll
;         for (int ai = 0; ai < 2; ++ai)
; #pragma unroll
;             for (int m = 0; m < 4; ++m) { bf16_t* rowp = O + (size_t)(row0 + ai * HALF + m * 16) * ldc + col0;
; #pragma unroll
;                 for (int bj = 0; bj < 2; ++bj) { const f32x4 v0 = acc[ai][bj][m][0], v1 = acc[ai][bj][m][1];
;                     u32x4 w; w.x = cvt_pk_bf16(v0[0], v0[1]); w.y = cvt_pk_bf16(v0[2], v0[3]); w.z = cvt_pk_bf16(v1[0], v1[1]); w.w = cvt_pk_bf16(v1[2], v1[3]);
;                     *(u32x4*)(rowp + bj * HALF) = w; } }
;     }
.LBB0_945:
	v_readlane_b32 s4, v251, 6
	v_lshl_or_b32 v140, s40, 8, v144
	v_readlane_b32 s5, v251, 7
	v_lshl_add_u32 v148, s41, 8, v142
	v_ashrrev_i32_e32 v141, 31, v140
	v_mov_b64_e32 v[138:139], s[4:5]
	v_mov_b32_e32 v150, s40
	v_lshlrev_b32_e32 v150, 13, v150
	v_lshl_add_u32 v150, v144, 5, v150
	v_and_b32_e32 v151, 15, v142
	v_lshl_add_u32 v150, v151, 4, v150
	v_add_u32_e32 v150, 0x800, v150
	v_mov_b32_e32 v151, 0
	v_lshl_add_u64 v[152:153], v[138:139], 0, v[150:151]
	v_and_b32_e32 v154, -16, v148
	v_lshlrev_b32_e32 v154, 12, v154
	v_mov_b32_e32 v155, 0
	v_mad_i64_i32 v[146:147], s[4:5], v148, s33, v[138:139]
	v_lshlrev_b64 v[140:141], 1, v[140:141]
	v_lshl_add_u64 v[146:147], v[146:147], 0, v[140:141]
	v_lshl_add_u64 v[146:147], v[154:155], 0, v[152:153]
	v_cvt_pk_bf16_f32 v124, v124, v125
	v_cvt_pk_bf16_f32 v125, v126, v127
	v_cvt_pk_bf16_f32 v126, v120, v121
	v_cvt_pk_bf16_f32 v127, v122, v123
	global_store_dwordx4 v[146:147], v[124:127], off offset:-2048
	v_cvt_pk_bf16_f32 v112, v112, v113
	v_cvt_pk_bf16_f32 v113, v114, v115
	v_cvt_pk_bf16_f32 v114, v104, v105
	v_or_b32_e32 v104, 16, v148
	v_and_b32_e32 v156, -16, v104
	v_lshlrev_b32_e32 v156, 12, v156
	v_mov_b32_e32 v157, 0
	v_mad_i64_i32 v[104:105], s[4:5], v104, s33, v[138:139]
	v_cvt_pk_bf16_f32 v115, v106, v107
	global_store_dwordx4 v[146:147], v[112:115], off offset:2048
	s_andn2_b64 vcc, exec, s[34:35]
	s_mov_b64 s[18:19], -1
	v_lshl_add_u64 v[112:113], v[104:105], 0, v[140:141]
	v_lshl_add_u64 v[112:113], v[156:157], 0, v[152:153]
	v_cvt_pk_bf16_f32 v104, v116, v117
	v_cvt_pk_bf16_f32 v105, v118, v119
	v_cvt_pk_bf16_f32 v106, v108, v109
	v_cvt_pk_bf16_f32 v107, v110, v111
	global_store_dwordx4 v[112:113], v[104:107], off offset:-2048
	v_cvt_pk_bf16_f32 v96, v96, v97
	v_cvt_pk_bf16_f32 v97, v98, v99
	v_cvt_pk_bf16_f32 v98, v88, v89
	v_or_b32_e32 v88, 32, v148
	v_and_b32_e32 v154, -16, v88
	v_lshlrev_b32_e32 v154, 12, v154
	v_mov_b32_e32 v155, 0
	v_mad_i64_i32 v[88:89], s[4:5], v88, s33, v[138:139]
	v_cvt_pk_bf16_f32 v99, v90, v91
	global_store_dwordx4 v[112:113], v[96:99], off offset:2048
	s_mov_b64 s[22:23], 0x800
	s_nop 0
	v_lshl_add_u64 v[96:97], v[88:89], 0, v[140:141]
	v_lshl_add_u64 v[96:97], v[154:155], 0, v[152:153]
	v_cvt_pk_bf16_f32 v88, v100, v101
	v_cvt_pk_bf16_f32 v89, v102, v103
	v_cvt_pk_bf16_f32 v90, v92, v93
	v_cvt_pk_bf16_f32 v91, v94, v95
	global_store_dwordx4 v[96:97], v[88:91], off offset:-2048
	v_cvt_pk_bf16_f32 v80, v80, v81
	v_cvt_pk_bf16_f32 v81, v82, v83
	v_cvt_pk_bf16_f32 v82, v72, v73
	v_or_b32_e32 v72, 48, v148
	v_and_b32_e32 v156, -16, v72
	v_lshlrev_b32_e32 v156, 12, v156
	v_mov_b32_e32 v157, 0
	v_mad_i64_i32 v[72:73], s[4:5], v72, s33, v[138:139]
	v_cvt_pk_bf16_f32 v83, v74, v75
	global_store_dwordx4 v[96:97], v[80:83], off offset:2048
	s_nop 1
	v_lshl_add_u64 v[80:81], v[72:73], 0, v[140:141]
	v_lshl_add_u64 v[80:81], v[156:157], 0, v[152:153]
	v_cvt_pk_bf16_f32 v72, v84, v85
	v_cvt_pk_bf16_f32 v73, v86, v87
	v_cvt_pk_bf16_f32 v74, v76, v77
	v_cvt_pk_bf16_f32 v75, v78, v79
	global_store_dwordx4 v[80:81], v[72:75], off offset:-2048
	v_cvt_pk_bf16_f32 v68, v68, v69
	v_cvt_pk_bf16_f32 v69, v70, v71
	v_cvt_pk_bf16_f32 v70, v64, v65
	v_add_u32_e32 v64, 0x80, v148
	v_and_b32_e32 v154, -16, v64
	v_lshlrev_b32_e32 v154, 12, v154
	v_mov_b32_e32 v155, 0
	v_mad_i64_i32 v[64:65], s[4:5], v64, s33, v[138:139]
	v_lshl_add_u64 v[64:65], v[64:65], 0, v[140:141]
	v_lshl_add_u64 v[64:65], v[154:155], 0, v[152:153]
	v_cvt_pk_bf16_f32 v71, v66, v67
	global_store_dwordx4 v[80:81], v[68:71], off offset:2048
	v_cvt_pk_bf16_f32 v60, v60, v61
	v_cvt_pk_bf16_f32 v61, v62, v63
	v_cvt_pk_bf16_f32 v62, v56, v57
	v_cvt_pk_bf16_f32 v63, v58, v59
	global_store_dwordx4 v[64:65], v[60:63], off offset:-2048
	v_cvt_pk_bf16_f32 v48, v48, v49
	v_cvt_pk_bf16_f32 v49, v50, v51
	v_cvt_pk_bf16_f32 v50, v40, v41
	v_add_u32_e32 v40, 0x90, v148
	v_and_b32_e32 v156, -16, v40
	v_lshlrev_b32_e32 v156, 12, v156
	v_mov_b32_e32 v157, 0
	v_mad_i64_i32 v[40:41], s[4:5], v40, s33, v[138:139]
	v_cvt_pk_bf16_f32 v51, v42, v43
	global_store_dwordx4 v[64:65], v[48:51], off offset:2048
	s_nop 1
	v_lshl_add_u64 v[48:49], v[40:41], 0, v[140:141]
	v_lshl_add_u64 v[48:49], v[156:157], 0, v[152:153]
	v_cvt_pk_bf16_f32 v40, v52, v53
	v_cvt_pk_bf16_f32 v41, v54, v55
	v_cvt_pk_bf16_f32 v42, v44, v45
	v_cvt_pk_bf16_f32 v43, v46, v47
	global_store_dwordx4 v[48:49], v[40:43], off offset:-2048
	v_cvt_pk_bf16_f32 v32, v32, v33
	v_cvt_pk_bf16_f32 v33, v34, v35
	v_cvt_pk_bf16_f32 v34, v24, v25
	v_add_u32_e32 v24, 0xa0, v148
	v_and_b32_e32 v154, -16, v24
	v_lshlrev_b32_e32 v154, 12, v154
	v_mov_b32_e32 v155, 0
	v_mad_i64_i32 v[24:25], s[4:5], v24, s33, v[138:139]
	v_cvt_pk_bf16_f32 v35, v26, v27
	global_store_dwordx4 v[48:49], v[32:35], off offset:2048
	s_nop 1
	v_lshl_add_u64 v[32:33], v[24:25], 0, v[140:141]
	v_lshl_add_u64 v[32:33], v[154:155], 0, v[152:153]
	v_cvt_pk_bf16_f32 v24, v36, v37
	v_cvt_pk_bf16_f32 v25, v38, v39
	v_cvt_pk_bf16_f32 v26, v28, v29
	v_cvt_pk_bf16_f32 v27, v30, v31
	global_store_dwordx4 v[32:33], v[24:27], off offset:-2048
	v_cvt_pk_bf16_f32 v16, v16, v17
	v_cvt_pk_bf16_f32 v17, v18, v19
	v_cvt_pk_bf16_f32 v18, v8, v9
	v_add_u32_e32 v8, 0xb0, v148
	v_and_b32_e32 v156, -16, v8
	v_lshlrev_b32_e32 v156, 12, v156
	v_mov_b32_e32 v157, 0
	v_mad_i64_i32 v[8:9], s[4:5], v8, s33, v[138:139]
	v_cvt_pk_bf16_f32 v19, v10, v11
	global_store_dwordx4 v[32:33], v[16:19], off offset:2048
	s_nop 1
	v_lshl_add_u64 v[16:17], v[8:9], 0, v[140:141]
	v_lshl_add_u64 v[16:17], v[156:157], 0, v[152:153]
	v_cvt_pk_bf16_f32 v8, v20, v21
	v_cvt_pk_bf16_f32 v9, v22, v23
	v_cvt_pk_bf16_f32 v10, v12, v13
	v_cvt_pk_bf16_f32 v11, v14, v15
	global_store_dwordx4 v[16:17], v[8:11], off offset:-2048
	v_cvt_pk_bf16_f32 v4, v4, v5
	v_cvt_pk_bf16_f32 v5, v6, v7
	v_cvt_pk_bf16_f32 v6, v0, v1
	v_cvt_pk_bf16_f32 v7, v2, v3
	global_store_dwordx4 v[16:17], v[4:7], off offset:2048
	s_cbranch_vccnz .LBB0_934
	s_andn2_b64 vcc, exec, s[0:1]
	s_cbranch_vccnz .LBB0_933
	s_barrier
	s_branch .LBB0_933

; #define GAS __attribute__((address_space(1)))
; #define LAS __attribute__((address_space(3)))
; __device__ __forceinline__ f32x4 mfma16(bf16x8 a, bf16x8 b, f32x4 c) { return __builtin_amdgcn_mfma_f32_16x16x32_bf16(a, b, c, 0, 0, 0); }
; __device__ __forceinline__ void topk_task(const Frame& F, int l, int tb, int h, const LAS unsigned char* kl, LAS float* tl, const LAS unsigned char* cab) {
;     ...
; #pragma unroll
;     for (int p = 0; p < 2; ++p)
; #pragma unroll
;         for (int ks = 0; ks < 4; ++ks) Qall[p][ks] = ld_b8(QP + (size_t)(t0 + c) * QPP + h * 256 + p * 128 + ks * 32 + rq * 8);
;     float rsp[8];
;     { const float* SS2 = (const float*)(F.ws + WS_SS2) + (t0 + c);
; #pragma unroll
;         for (int i = 0; i < 8; ++i) rsp[i] = *(const GAS float*)(SS2 + (size_t)(rq * 8 + i) * T); }
; #pragma unroll
;     for (int p = 0; p < 2; ++p) {
;         bf16x8 Qf[4];
; #pragma unroll
;         for (int ks = 0; ks < 4; ++ks) Qf[ks] = Qall[p][ks];
;         float v[32];
;         const LAS unsigned char* kbase = kl + (p * 128 + c) * KL_PITCH + rq * 16;
; #pragma unroll
;         for (int kb = 0; kb < 8; ++kb) {
;             f32x4 a = (f32x4){0.f, 0.f, 0.f, 0.f};
; #pragma unroll
;             for (int ks = 0; ks < 4; ++ks) a = mfma16(*(const LAS bf16x8*)(kbase + kb * 16 * KL_PITCH + ks * 64), Qf[ks], a);
; #pragma unroll
;             for (int e = 0; e < 4; ++e) v[kb * 4 + e] = embed_idx<127u>(a[e], (unsigned)(kb * 16 + rq * 4 + e));
; __global__ void __launch_bounds__(NWAVES * 64, 2) hybrid_fwd(Args args) {
;     ...
;                     __syncthreads();
; #pragma unroll
;                     for (int i = 0; i < 8; ++i) { const int idx = tid3 + 512 * i, row = idx >> 4, c16 = idx & 15;
;                         *(LAS u32x4*)(kl + row * KL_PITCH + c16 * 16) = ld_u4(KEYS + ((size_t)h * 256 + row) * 128 + c16 * 8); }
;                     __syncthreads();
.LBB0_1009:
	v_lshl_add_u64 v[0:1], s[62:63], 0, v[66:67]
	v_add_co_u32_e32 v0, vcc, 0x300000, v0
	s_nop 1
	v_addc_co_u32_e32 v1, vcc, 0, v1, vcc
	s_barrier
	global_load_dwordx4 v[0:3], v[0:1], off
	v_mov_b32_e32 v90, v211
	s_waitcnt vmcnt(0)
	ds_write_b128 v72, v[0:3]
	v_lshl_add_u64 v[0:1], s[62:63], 0, v[64:65]
	v_add_co_u32_e32 v0, vcc, 0x300000, v0
	s_nop 1
	v_addc_co_u32_e32 v1, vcc, 0, v1, vcc
	global_load_dwordx4 v[0:3], v[0:1], off
	s_waitcnt vmcnt(0)
	ds_write_b128 v73, v[0:3]
	v_lshl_add_u64 v[0:1], s[62:63], 0, v[62:63]
	v_add_co_u32_e32 v0, vcc, 0x300000, v0
	s_nop 1
	v_addc_co_u32_e32 v1, vcc, 0, v1, vcc
	global_load_dwordx4 v[0:3], v[0:1], off
	s_waitcnt vmcnt(0)
	ds_write_b128 v74, v[0:3]
	v_lshl_add_u64 v[0:1], s[62:63], 0, v[60:61]
	v_add_co_u32_e32 v0, vcc, 0x300000, v0
	s_nop 1
	v_addc_co_u32_e32 v1, vcc, 0, v1, vcc
	global_load_dwordx4 v[0:3], v[0:1], off
	s_waitcnt vmcnt(0)
	ds_write_b128 v75, v[0:3]
	v_lshl_add_u64 v[0:1], s[62:63], 0, v[58:59]
	v_add_co_u32_e32 v0, vcc, 0x300000, v0
	s_nop 1
	v_addc_co_u32_e32 v1, vcc, 0, v1, vcc
	global_load_dwordx4 v[0:3], v[0:1], off
	s_waitcnt vmcnt(0)
	ds_write_b128 v76, v[0:3]
	v_lshl_add_u64 v[0:1], s[62:63], 0, v[56:57]
	v_add_co_u32_e32 v0, vcc, 0x300000, v0
	s_nop 1
	v_addc_co_u32_e32 v1, vcc, 0, v1, vcc
	global_load_dwordx4 v[0:3], v[0:1], off
	s_waitcnt vmcnt(0)
	ds_write_b128 v77, v[0:3]
	v_lshl_add_u64 v[0:1], s[62:63], 0, v[54:55]
	v_add_co_u32_e32 v0, vcc, 0x300000, v0
	s_nop 1
	v_addc_co_u32_e32 v1, vcc, 0, v1, vcc
	global_load_dwordx4 v[0:3], v[0:1], off
	s_waitcnt vmcnt(0)
	ds_write_b128 v78, v[0:3]
	v_lshl_add_u64 v[0:1], s[62:63], 0, v[52:53]
	v_add_co_u32_e32 v0, vcc, 0x300000, v0
	s_nop 1
	v_addc_co_u32_e32 v1, vcc, 0, v1, vcc
	global_load_dwordx4 v[0:3], v[0:1], off
	s_waitcnt vmcnt(0)
	ds_write_b128 v79, v[0:3]
	s_waitcnt lgkmcnt(0)
	s_barrier
	s_nop 0
	v_ashrrev_i32_e32 v80, 4, v90
	v_lshlrev_b32_e32 v34, 3, v80
	v_and_b32_e32 v88, 15, v90
	v_ashrrev_i32_e32 v35, 31, v34
	v_add_u32_e32 v68, s24, v88
	v_lshlrev_b64 v[0:1], 1, v[34:35]
	v_mad_i64_i32 v[0:1], s[0:1], v68, s33, v[0:1]
	s_add_u32 s0, s62, s17
	s_addc_u32 s1, s63, s22
	v_lshl_add_u64 v[0:1], s[0:1], 0, v[0:1]
	s_mov_b32 s0, 0x32c00000
	v_add_co_u32_e32 v0, vcc, s0, v0
	v_or_b32_e32 v32, s23, v88
	s_nop 0
	v_addc_co_u32_e32 v1, vcc, 0, v1, vcc
	v_lshlrev_b32_e32 v226, 4, v88
	v_lshl_add_u32 v226, v80, 8, v226
	v_lshl_add_u32 v226, s24, 12, v226
	v_lshl_add_u32 v226, s17, 4, v226
	v_add_u32_e32 v226, 0x32c00000, v226
	v_mov_b32_e32 v227, 0
	v_lshl_add_u64 v[0:1], s[62:63], 0, v[226:227]
	v_mov_b32_e32 v226, 0x1000
	v_lshl_add_u64 v[228:229], v[0:1], 0, v[226:227]
	global_load_dwordx4 v[28:31], v[0:1], off
	global_load_dwordx4 v[24:27], v[0:1], off offset:1024
	global_load_dwordx4 v[20:23], v[0:1], off offset:2048
	global_load_dwordx4 v[16:19], v[0:1], off offset:3072
	global_load_dwordx4 v[12:15], v[228:229], off
	global_load_dwordx4 v[8:11], v[228:229], off offset:1024
	global_load_dwordx4 v[4:7], v[228:229], off offset:2048
	s_nop 0
	global_load_dwordx4 v[0:3], v[228:229], off offset:3072
	v_ashrrev_i32_e32 v33, 31, v32
	v_lshl_add_u64 v[32:33], v[32:33], 2, s[40:41]
	v_lshlrev_b64 v[82:83], 16, v[34:35]
	v_lshl_add_u64 v[82:83], v[32:33], 0, v[82:83]
	global_load_dword v69, v[82:83], off
	v_or_b32_e32 v82, 1, v34
	v_ashrrev_i32_e32 v83, 31, v82
	v_lshlrev_b64 v[82:83], 16, v[82:83]
	v_lshl_add_u64 v[82:83], v[32:33], 0, v[82:83]
	global_load_dword v81, v[82:83], off
	v_or_b32_e32 v82, 2, v34
	v_or_b32_e32 v84, 3, v34
	v_ashrrev_i32_e32 v83, 31, v82
	v_ashrrev_i32_e32 v85, 31, v84
	v_lshlrev_b64 v[82:83], 16, v[82:83]
	v_lshlrev_b64 v[84:85], 16, v[84:85]
	v_lshl_add_u64 v[82:83], v[32:33], 0, v[82:83]
	v_lshl_add_u64 v[84:85], v[32:33], 0, v[84:85]
	global_load_dword v82, v[82:83], off
	v_or_b32_e32 v86, 5, v34
	global_load_dword v83, v[84:85], off
	v_or_b32_e32 v84, 4, v34
	v_ashrrev_i32_e32 v85, 31, v84
	v_ashrrev_i32_e32 v87, 31, v86
	v_lshlrev_b64 v[84:85], 16, v[84:85]
	v_lshlrev_b64 v[86:87], 16, v[86:87]
	v_lshl_add_u64 v[84:85], v[32:33], 0, v[84:85]
	v_lshl_add_u64 v[86:87], v[32:33], 0, v[86:87]
	global_load_dword v84, v[84:85], off
	v_lshlrev_b32_e32 v91, 2, v80
	global_load_dword v85, v[86:87], off
	v_or_b32_e32 v86, 6, v34
	v_or_b32_e32 v34, 7, v34
	v_ashrrev_i32_e32 v87, 31, v86
	v_ashrrev_i32_e32 v35, 31, v34
	v_lshlrev_b64 v[86:87], 16, v[86:87]
	v_lshlrev_b64 v[34:35], 16, v[34:35]
	v_lshl_add_u64 v[86:87], v[32:33], 0, v[86:87]
	v_lshl_add_u64 v[32:33], v[32:33], 0, v[34:35]
	global_load_dword v86, v[86:87], off
	v_or_b32_e32 v97, 1, v91
	global_load_dword v87, v[32:33], off
	v_and_b32_e32 v32, -16, v90
	v_mul_u32_u24_e32 v33, 0x110, v88
	v_add3_u32 v89, 0, v32, v33
	ds_read_b128 v[32:35], v89
	ds_read_b128 v[92:95], v89 offset:64
	s_waitcnt vmcnt(15) lgkmcnt(1)
	v_mfma_f32_16x16x32_bf16 v[32:35], v[32:35], v[28:31], 0
	ds_read_b128 v[108:111], v89 offset:4416
	ds_read_b128 v[116:119], v89 offset:13120
	v_sub_u32_e32 v98, 0x7f, v97
	s_waitcnt vmcnt(14) lgkmcnt(2)
	v_mfma_f32_16x16x32_bf16 v[32:35], v[92:95], v[24:27], v[32:35]
	ds_read_b128 v[92:95], v89 offset:128
	v_or_b32_e32 v103, 2, v91
	v_sub_u32_e32 v104, 0x7f, v103
	s_waitcnt vmcnt(13) lgkmcnt(0)
	v_mfma_f32_16x16x32_bf16 v[32:35], v[92:95], v[20:23], v[32:35]
	ds_read_b128 v[92:95], v89 offset:192
	v_or_b32_e32 v105, 3, v91
	v_sub_u32_e32 v106, 0x7f, v105
	s_waitcnt vmcnt(12) lgkmcnt(0)
; #define LAS __attribute__((address_space(3)))
; __device__ __forceinline__ f32x4 mfma16(bf16x8 a, bf16x8 b, f32x4 c) { return __builtin_amdgcn_mfma_f32_16x16x32_bf16(a, b, c, 0, 0, 0); }
; __device__ __forceinline__ void topk_task(const Frame& F, int l, int tb, int h, const LAS unsigned char* kl, LAS float* tl, const LAS unsigned char* cab) {
;     ...
; #pragma unroll
;         for (int kb = 0; kb < 8; ++kb) {
;             f32x4 a = (f32x4){0.f, 0.f, 0.f, 0.f};
; #pragma unroll
;             for (int ks = 0; ks < 4; ++ks) a = mfma16(*(const LAS bf16x8*)(kbase + kb * 16 * KL_PITCH + ks * 64), Qf[ks], a);
; #pragma unroll
;             for (int e = 0; e < 4; ++e) v[kb * 4 + e] = embed_idx<127u>(a[e], (unsigned)(kb * 16 + rq * 4 + e));
;         }
	v_mfma_f32_16x16x32_bf16 v[32:35], v[92:95], v[16:19], v[32:35]
	v_sub_u32_e32 v94, 0x7f, v91
	ds_read_b128 v[124:127], v89 offset:17472
	ds_read_b128 v[132:135], v89 offset:21824
	s_nop 4
	v_cmp_gt_i32_e32 vcc, 0, v32
	ds_read_b128 v[164:167], v89 offset:26176
	v_sub_u32_e32 v93, 0x6f, v91
	v_cndmask_b32_e32 v92, v94, v91, vcc
	v_cmp_gt_i32_e32 vcc, 0, v33
	v_and_or_b32 v143, v32, s79, v92
	v_add_u32_e32 v92, 16, v91
	v_cndmask_b32_e32 v32, v98, v97, vcc
	v_cmp_gt_i32_e32 vcc, 0, v34
	v_and_or_b32 v144, v33, s79, v32
	v_sub_u32_e32 v96, 0x6e, v91
	v_cndmask_b32_e32 v32, v104, v103, vcc
	v_cmp_gt_i32_e32 vcc, 0, v35
	v_and_or_b32 v145, v34, s79, v32
	v_add_u32_e32 v99, 18, v91
	v_cndmask_b32_e32 v32, v106, v105, vcc
	v_and_or_b32 v146, v35, s79, v32
	ds_read_b128 v[32:35], v89 offset:4352
	s_waitcnt lgkmcnt(0)
	v_mfma_f32_16x16x32_bf16 v[32:35], v[32:35], v[28:31], 0
	v_sub_u32_e32 v100, 0x6d, v91
	v_add_u32_e32 v101, 19, v91
	v_sub_u32_e32 v102, 0x6c, v91
	v_mfma_f32_16x16x32_bf16 v[32:35], v[108:111], v[24:27], v[32:35]
	ds_read_b128 v[108:111], v89 offset:4480
	v_sub_u32_e32 v140, 29, v91
	v_sub_u32_e32 v142, 28, v91
	s_waitcnt lgkmcnt(0)
	v_mfma_f32_16x16x32_bf16 v[32:35], v[108:111], v[20:23], v[32:35]
	ds_read_b128 v[108:111], v89 offset:4544
	v_cmp_gt_u32_e64 s[34:35], 16, v90
	s_waitcnt lgkmcnt(0)
	v_mfma_f32_16x16x32_bf16 v[32:35], v[108:111], v[16:19], v[32:35]
	ds_read_b128 v[108:111], v89 offset:8768
	s_nop 6
	v_cmp_gt_i32_e32 vcc, 0, v32
	s_nop 1
	v_cndmask_b32_e32 v95, v93, v92, vcc
	v_and_or_b32 v147, v32, s79, v95
	v_add_u32_e32 v95, 17, v91
	v_cmp_gt_i32_e32 vcc, 0, v33
	s_nop 1
	v_cndmask_b32_e32 v32, v96, v95, vcc
	v_cmp_gt_i32_e32 vcc, 0, v34
	v_and_or_b32 v148, v33, s79, v32
	s_nop 0
	v_cndmask_b32_e32 v32, v100, v99, vcc
	v_cmp_gt_i32_e32 vcc, 0, v35
	v_and_or_b32 v149, v34, s79, v32
	s_nop 0
	v_cndmask_b32_e32 v32, v102, v101, vcc
	v_and_or_b32 v150, v35, s79, v32
	ds_read_b128 v[32:35], v89 offset:8704
	s_waitcnt lgkmcnt(0)
	v_mfma_f32_16x16x32_bf16 v[32:35], v[32:35], v[28:31], 0
	v_mfma_f32_16x16x32_bf16 v[32:35], v[108:111], v[24:27], v[32:35]
	ds_read_b128 v[108:111], v89 offset:8832
	s_waitcnt lgkmcnt(0)
	v_mfma_f32_16x16x32_bf16 v[32:35], v[108:111], v[20:23], v[32:35]
	ds_read_b128 v[108:111], v89 offset:8896
	s_waitcnt lgkmcnt(0)
	v_mfma_f32_16x16x32_bf16 v[108:111], v[108:111], v[16:19], v[32:35]
	s_nop 4
	v_add_u32_e32 v32, 32, v91
	v_sub_u32_e32 v33, 0x5f, v91
	v_sub_u32_e32 v35, 0x5e, v91
	v_cmp_gt_i32_e32 vcc, 0, v108
	s_nop 1
	v_cndmask_b32_e32 v34, v33, v32, vcc
	v_and_or_b32 v151, v108, s79, v34
	v_add_u32_e32 v34, 33, v91
	v_cmp_gt_i32_e32 vcc, 0, v109
	v_sub_u32_e32 v108, 0x5d, v91
	s_nop 0
	v_cndmask_b32_e32 v107, v35, v34, vcc
	v_and_or_b32 v152, v109, s79, v107
	v_add_u32_e32 v107, 34, v91
	v_cmp_gt_i32_e32 vcc, 0, v110
	s_nop 1
	v_cndmask_b32_e32 v109, v108, v107, vcc
	v_and_or_b32 v153, v110, s79, v109
	v_add_u32_e32 v109, 35, v91
	v_sub_u32_e32 v110, 0x5c, v91
	v_cmp_gt_i32_e32 vcc, 0, v111
	s_nop 1
	v_cndmask_b32_e32 v112, v110, v109, vcc
	v_and_or_b32 v154, v111, s79, v112
	ds_read_b128 v[112:115], v89 offset:13056
	s_waitcnt lgkmcnt(0)
	v_mfma_f32_16x16x32_bf16 v[112:115], v[112:115], v[28:31], 0
	v_add_u32_e32 v111, 48, v91
	v_mfma_f32_16x16x32_bf16 v[112:115], v[116:119], v[24:27], v[112:115]
	ds_read_b128 v[116:119], v89 offset:13184
	s_waitcnt lgkmcnt(0)
	v_mfma_f32_16x16x32_bf16 v[112:115], v[116:119], v[20:23], v[112:115]
	ds_read_b128 v[116:119], v89 offset:13248
	s_waitcnt lgkmcnt(0)
	v_mfma_f32_16x16x32_bf16 v[116:119], v[116:119], v[16:19], v[112:115]
	s_nop 4
	v_sub_u32_e32 v112, 0x4f, v91
	v_sub_u32_e32 v114, 0x4e, v91
	s_nop 0
	v_cmp_gt_i32_e32 vcc, 0, v116
	s_nop 1
	v_cndmask_b32_e32 v113, v112, v111, vcc
	v_and_or_b32 v155, v116, s79, v113
	v_add_u32_e32 v113, 49, v91
	v_cmp_gt_i32_e32 vcc, 0, v117
	v_sub_u32_e32 v116, 0x4d, v91
	s_nop 0
	v_cndmask_b32_e32 v115, v114, v113, vcc
	v_and_or_b32 v156, v117, s79, v115
	v_add_u32_e32 v115, 50, v91
	v_cmp_gt_i32_e32 vcc, 0, v118
	s_nop 1
	v_cndmask_b32_e32 v117, v116, v115, vcc
	v_and_or_b32 v157, v118, s79, v117
	v_add_u32_e32 v117, 51, v91
	v_sub_u32_e32 v118, 0x4c, v91
	v_cmp_gt_i32_e32 vcc, 0, v119
	s_nop 1
	v_cndmask_b32_e32 v120, v118, v117, vcc
	v_and_or_b32 v158, v119, s79, v120
	ds_read_b128 v[120:123], v89 offset:17408
	s_waitcnt lgkmcnt(0)
	v_mfma_f32_16x16x32_bf16 v[120:123], v[120:123], v[28:31], 0
	v_add_u32_e32 v119, 64, v91
	v_mfma_f32_16x16x32_bf16 v[120:123], v[124:127], v[24:27], v[120:123]
	ds_read_b128 v[124:127], v89 offset:17536
	s_waitcnt lgkmcnt(0)
	v_mfma_f32_16x16x32_bf16 v[120:123], v[124:127], v[20:23], v[120:123]
	ds_read_b128 v[124:127], v89 offset:17600
	s_waitcnt lgkmcnt(0)
	v_mfma_f32_16x16x32_bf16 v[124:127], v[124:127], v[16:19], v[120:123]
	s_nop 4
	v_sub_u32_e32 v120, 63, v91
	v_sub_u32_e32 v122, 62, v91
	s_nop 0
	v_cmp_gt_i32_e32 vcc, 0, v124
	s_nop 1
	v_cndmask_b32_e32 v121, v120, v119, vcc
	v_and_or_b32 v159, v124, s79, v121
	v_add_u32_e32 v121, 0x41, v91
	v_cmp_gt_i32_e32 vcc, 0, v125
	v_sub_u32_e32 v124, 61, v91
	s_nop 0
	v_cndmask_b32_e32 v123, v122, v121, vcc
	v_and_or_b32 v160, v125, s79, v123
	v_add_u32_e32 v123, 0x42, v91
	v_cmp_gt_i32_e32 vcc, 0, v126
	s_nop 1
	v_cndmask_b32_e32 v125, v124, v123, vcc
	v_and_or_b32 v161, v126, s79, v125
	v_add_u32_e32 v125, 0x43, v91
	v_sub_u32_e32 v126, 60, v91
	v_cmp_gt_i32_e32 vcc, 0, v127
	s_nop 1
	v_cndmask_b32_e32 v128, v126, v125, vcc
	v_and_or_b32 v162, v127, s79, v128
	ds_read_b128 v[128:131], v89 offset:21760
	s_waitcnt lgkmcnt(0)
; #define LAS __attribute__((address_space(3)))
; __device__ __forceinline__ f32x4 mfma16(bf16x8 a, bf16x8 b, f32x4 c) { return __builtin_amdgcn_mfma_f32_16x16x32_bf16(a, b, c, 0, 0, 0); }
; template <int N> __device__ __forceinline__ void sortdesc(float (&v)[N]) {
; #pragma unroll
;     for (int k = 2; k <= N; k <<= 1)
; #pragma unroll
;         for (int j = k >> 1; j > 0; j >>= 1)
; #pragma unroll
;             for (int i = 0; i < N; ++i) { const int p = i ^ j;
;                 if (p > i) { const bool desc = ((i & k) == 0); const float a = v[i], b = v[p], hi = fmaxf(a, b), lo = fminf(a, b); v[i] = desc ? hi : lo; v[p] = desc ? lo : hi; } }
; }
; __device__ __forceinline__ void topk_task(const Frame& F, int l, int tb, int h, const LAS unsigned char* kl, LAS float* tl, const LAS unsigned char* cab) {
;     ...
; #pragma unroll
;         for (int kb = 0; kb < 8; ++kb) {
;             f32x4 a = (f32x4){0.f, 0.f, 0.f, 0.f};
; #pragma unroll
;             for (int ks = 0; ks < 4; ++ks) a = mfma16(*(const LAS bf16x8*)(kbase + kb * 16 * KL_PITCH + ks * 64), Qf[ks], a);
; #pragma unroll
;             for (int e = 0; e < 4; ++e) v[kb * 4 + e] = embed_idx<127u>(a[e], (unsigned)(kb * 16 + rq * 4 + e));
;         }
;         sortdesc<32>(v);
	v_mfma_f32_16x16x32_bf16 v[128:131], v[128:131], v[28:31], 0
	v_add_u32_e32 v127, 0x50, v91
	v_mfma_f32_16x16x32_bf16 v[128:131], v[132:135], v[24:27], v[128:131]
	ds_read_b128 v[132:135], v89 offset:21888
	s_waitcnt lgkmcnt(0)
	v_mfma_f32_16x16x32_bf16 v[128:131], v[132:135], v[20:23], v[128:131]
	ds_read_b128 v[132:135], v89 offset:21952
	s_waitcnt lgkmcnt(0)
	v_mfma_f32_16x16x32_bf16 v[132:135], v[132:135], v[16:19], v[128:131]
	s_nop 4
	v_sub_u32_e32 v128, 47, v91
	v_sub_u32_e32 v130, 46, v91
	s_nop 0
	v_cmp_gt_i32_e32 vcc, 0, v132
	s_nop 1
	v_cndmask_b32_e32 v129, v128, v127, vcc
	v_and_or_b32 v163, v132, s79, v129
	v_add_u32_e32 v129, 0x51, v91
	v_cmp_gt_i32_e32 vcc, 0, v133
	v_sub_u32_e32 v132, 45, v91
	s_nop 0
	v_cndmask_b32_e32 v131, v130, v129, vcc
	v_and_or_b32 v168, v133, s79, v131
	v_add_u32_e32 v131, 0x52, v91
	v_cmp_gt_i32_e32 vcc, 0, v134
	s_nop 1
	v_cndmask_b32_e32 v133, v132, v131, vcc
	v_and_or_b32 v169, v134, s79, v133
	v_add_u32_e32 v133, 0x53, v91
	v_sub_u32_e32 v134, 44, v91
	v_cmp_gt_i32_e32 vcc, 0, v135
	s_nop 1
	v_cndmask_b32_e32 v136, v134, v133, vcc
	v_and_or_b32 v170, v135, s79, v136
	ds_read_b128 v[136:139], v89 offset:26112
	s_waitcnt lgkmcnt(0)
	v_mfma_f32_16x16x32_bf16 v[136:139], v[136:139], v[28:31], 0
	v_add_u32_e32 v135, 0x60, v91
	v_mfma_f32_16x16x32_bf16 v[136:139], v[164:167], v[24:27], v[136:139]
	ds_read_b128 v[164:167], v89 offset:26240
	s_waitcnt lgkmcnt(0)
	v_mfma_f32_16x16x32_bf16 v[136:139], v[164:167], v[20:23], v[136:139]
	ds_read_b128 v[164:167], v89 offset:26304
	s_waitcnt lgkmcnt(0)
	v_mfma_f32_16x16x32_bf16 v[164:167], v[164:167], v[16:19], v[136:139]
	s_nop 4
	v_sub_u32_e32 v136, 31, v91
	v_sub_u32_e32 v138, 30, v91
	s_nop 0
	v_cmp_gt_i32_e32 vcc, 0, v164
	s_nop 1
	v_cndmask_b32_e32 v137, v136, v135, vcc
	v_and_or_b32 v171, v164, s79, v137
	v_add_u32_e32 v137, 0x61, v91
	v_cmp_gt_i32_e32 vcc, 0, v165
	s_nop 1
	v_cndmask_b32_e32 v139, v138, v137, vcc
	v_and_or_b32 v172, v165, s79, v139
	v_add_u32_e32 v139, 0x62, v91
	v_cmp_gt_i32_e32 vcc, 0, v166
	s_nop 1
	v_cndmask_b32_e32 v141, v140, v139, vcc
	v_and_or_b32 v173, v166, s79, v141
	v_add_u32_e32 v141, 0x63, v91
	v_cmp_gt_i32_e32 vcc, 0, v167
	s_nop 1
	v_cndmask_b32_e32 v164, v142, v141, vcc
	v_and_or_b32 v174, v167, s79, v164
	ds_read_b128 v[164:167], v89 offset:30464
	s_waitcnt lgkmcnt(0)
	v_mfma_f32_16x16x32_bf16 v[28:31], v[164:167], v[28:31], 0
	ds_read_b128 v[164:167], v89 offset:30528
	s_waitcnt lgkmcnt(0)
	v_mfma_f32_16x16x32_bf16 v[24:27], v[164:167], v[24:27], v[28:31]
	s_nop 4
	ds_read_b128 v[28:31], v89 offset:30592
	v_max_f32_e32 v164, v171, v171
	v_max_f32_e32 v166, v173, v173
	s_waitcnt lgkmcnt(0)
	v_mfma_f32_16x16x32_bf16 v[20:23], v[28:31], v[20:23], v[24:27]
	s_nop 2
	ds_read_b128 v[24:27], v89 offset:30656
	v_max_f32_e32 v29, v143, v143
	v_max_f32_e32 v31, v145, v145
	s_waitcnt lgkmcnt(0)
	v_mfma_f32_16x16x32_bf16 v[22:25], v[24:27], v[16:19], v[20:23]
	v_add_u32_e32 v17, 0x70, v91
	v_sub_u32_e32 v18, 15, v91
	v_add_u32_e32 v19, 0x71, v91
	s_nop 4
	v_cmp_gt_i32_e32 vcc, 0, v22
	v_sub_u32_e32 v20, 14, v91
	s_nop 0
	v_cndmask_b32_e32 v16, v18, v17, vcc
	v_cmp_gt_i32_e32 vcc, 0, v23
	v_and_or_b32 v16, v22, s79, v16
	v_sub_u32_e32 v22, 13, v91
	v_cndmask_b32_e32 v21, v20, v19, vcc
	v_and_or_b32 v26, v23, s79, v21
	v_add_u32_e32 v21, 0x72, v91
	v_cmp_gt_i32_e32 vcc, 0, v24
	v_max_f32_e32 v26, v26, v26
	v_max_f32_e32 v16, v16, v16
	v_cndmask_b32_e32 v23, v22, v21, vcc
	v_and_or_b32 v27, v24, s79, v23
	v_add_u32_e32 v23, 0x73, v91
	v_sub_u32_e32 v24, 12, v91
	v_cmp_gt_i32_e32 vcc, 0, v25
	s_nop 1
	v_cndmask_b32_e32 v28, v24, v23, vcc
	v_and_or_b32 v25, v25, s79, v28
	v_max_f32_e32 v28, v144, v144
	v_max_f32_e32 v30, v29, v28
	v_min_f32_e32 v28, v29, v28
	v_max_f32_e32 v29, v146, v146
	v_max_f32_e32 v143, v31, v29
	v_min_f32_e32 v29, v31, v29
	v_max_f32_e32 v31, v148, v148
	v_max_f32_e32 v144, v147, v147
	v_max_f32_e32 v145, v144, v31
	v_min_f32_e32 v31, v144, v31
	v_max_f32_e32 v144, v150, v150
	v_max_f32_e32 v146, v149, v149
	v_max_f32_e32 v147, v146, v144
	v_min_f32_e32 v144, v146, v144
	v_max_f32_e32 v146, v152, v152
	v_max_f32_e32 v148, v151, v151
	v_max_f32_e32 v149, v148, v146
	v_min_f32_e32 v146, v148, v146
	v_max_f32_e32 v148, v154, v154
	v_max_f32_e32 v150, v153, v153
	v_max_f32_e32 v151, v150, v148
	v_min_f32_e32 v148, v150, v148
	v_max_f32_e32 v150, v156, v156
	v_max_f32_e32 v152, v155, v155
	v_max_f32_e32 v153, v152, v150
	v_min_f32_e32 v150, v152, v150
	v_max_f32_e32 v152, v158, v158
	v_max_f32_e32 v154, v157, v157
	v_max_f32_e32 v155, v154, v152
	v_min_f32_e32 v152, v154, v152
	v_max_f32_e32 v154, v160, v160
	v_max_f32_e32 v156, v159, v159
	v_max_f32_e32 v157, v156, v154
	v_min_f32_e32 v154, v156, v154
	v_max_f32_e32 v156, v162, v162
	v_max_f32_e32 v158, v161, v161
	v_max_f32_e32 v159, v158, v156
	v_min_f32_e32 v156, v158, v156
	v_max_f32_e32 v158, v168, v168
	v_max_f32_e32 v160, v163, v163
	v_max_f32_e32 v161, v160, v158
	v_min_f32_e32 v158, v160, v158
	v_max_f32_e32 v160, v170, v170
	v_max_f32_e32 v162, v169, v169
	v_max_f32_e32 v163, v162, v160
	v_min_f32_e32 v160, v162, v160
	v_max_f32_e32 v162, v172, v172
	v_max_f32_e32 v165, v164, v162
	v_min_f32_e32 v162, v164, v162
	v_max_f32_e32 v164, v174, v174
	v_max_f32_e32 v167, v166, v164
	v_min_f32_e32 v164, v166, v164
	v_max_f32_e32 v166, v16, v26
	v_min_f32_e32 v16, v16, v26
	v_max_f32_e32 v25, v25, v25
	v_max_f32_e32 v26, v27, v27
	v_max_f32_e32 v27, v26, v25
	v_min_f32_e32 v25, v26, v25
	v_max_f32_e32 v26, v30, v29
	v_min_f32_e32 v29, v30, v29
	v_max_f32_e32 v30, v28, v143
	v_min_f32_e32 v28, v28, v143
	v_max_f32_e32 v143, v145, v144
	v_min_f32_e32 v144, v145, v144
; template <int N> __device__ __forceinline__ void sortdesc(float (&v)[N]) {
; #pragma unroll
;     for (int k = 2; k <= N; k <<= 1)
; #pragma unroll
;         for (int j = k >> 1; j > 0; j >>= 1)
; #pragma unroll
;             for (int i = 0; i < N; ++i) { const int p = i ^ j;
;                 if (p > i) { const bool desc = ((i & k) == 0); const float a = v[i], b = v[p], hi = fmaxf(a, b), lo = fminf(a, b); v[i] = desc ? hi : lo; v[p] = desc ? lo : hi; } }
; }
	v_max_f32_e32 v145, v31, v147
	v_min_f32_e32 v31, v31, v147
	v_max_f32_e32 v147, v149, v148
	v_min_f32_e32 v148, v149, v148
	v_max_f32_e32 v149, v146, v151
	v_min_f32_e32 v146, v146, v151
	v_max_f32_e32 v151, v153, v152
	v_min_f32_e32 v152, v153, v152
	v_max_f32_e32 v153, v150, v155
	v_min_f32_e32 v150, v150, v155
	v_max_f32_e32 v155, v157, v156
	v_min_f32_e32 v156, v157, v156
	v_max_f32_e32 v157, v154, v159
	v_min_f32_e32 v154, v154, v159
	v_max_f32_e32 v159, v161, v160
	v_min_f32_e32 v160, v161, v160
	v_max_f32_e32 v161, v158, v163
	v_min_f32_e32 v158, v158, v163
	v_max_f32_e32 v163, v165, v164
	v_min_f32_e32 v164, v165, v164
	v_max_f32_e32 v165, v162, v167
	v_min_f32_e32 v162, v162, v167
	v_max_f32_e32 v167, v166, v25
	v_min_f32_e32 v25, v166, v25
	v_max_f32_e32 v166, v16, v27
	v_min_f32_e32 v16, v16, v27
	v_max_f32_e32 v27, v26, v30
	v_min_f32_e32 v26, v26, v30
	v_max_f32_e32 v30, v29, v28
	v_min_f32_e32 v28, v29, v28
	v_max_f32_e32 v29, v144, v31
	v_min_f32_e32 v31, v144, v31
	v_max_f32_e32 v144, v143, v145
	v_min_f32_e32 v143, v143, v145
	v_max_f32_e32 v145, v147, v149
	v_min_f32_e32 v147, v147, v149
	v_max_f32_e32 v149, v148, v146
	v_min_f32_e32 v146, v148, v146
	v_max_f32_e32 v148, v152, v150
	v_min_f32_e32 v150, v152, v150
	v_max_f32_e32 v152, v151, v153
	v_min_f32_e32 v151, v151, v153
	v_max_f32_e32 v153, v155, v157
	v_min_f32_e32 v155, v155, v157
	v_max_f32_e32 v157, v156, v154
	v_min_f32_e32 v154, v156, v154
	v_max_f32_e32 v156, v160, v158
	v_min_f32_e32 v158, v160, v158
	v_max_f32_e32 v160, v159, v161
	v_min_f32_e32 v159, v159, v161
	v_max_f32_e32 v161, v163, v165
	v_min_f32_e32 v163, v163, v165
	v_max_f32_e32 v165, v164, v162
	v_min_f32_e32 v162, v164, v162
	v_max_f32_e32 v164, v25, v16
	v_min_f32_e32 v16, v25, v16
	v_max_f32_e32 v25, v167, v166
	v_min_f32_e32 v166, v167, v166
	v_max_f32_e32 v167, v27, v31
	v_min_f32_e32 v27, v27, v31
	v_max_f32_e32 v31, v26, v29
	v_min_f32_e32 v26, v26, v29
	v_max_f32_e32 v29, v30, v143
	v_min_f32_e32 v30, v30, v143
	v_max_f32_e32 v143, v28, v144
	v_min_f32_e32 v28, v28, v144
	v_max_f32_e32 v144, v145, v150
	v_min_f32_e32 v145, v145, v150
	v_max_f32_e32 v150, v147, v148
	v_min_f32_e32 v147, v147, v148
	v_max_f32_e32 v148, v149, v151
	v_min_f32_e32 v149, v149, v151
	v_max_f32_e32 v151, v146, v152
	v_min_f32_e32 v146, v146, v152
	v_max_f32_e32 v152, v153, v158
	v_min_f32_e32 v153, v153, v158
	v_max_f32_e32 v158, v155, v156
	v_min_f32_e32 v155, v155, v156
	v_max_f32_e32 v156, v157, v159
	v_min_f32_e32 v157, v157, v159
	v_max_f32_e32 v159, v154, v160
	v_min_f32_e32 v154, v154, v160
	v_max_f32_e32 v160, v161, v16
	v_min_f32_e32 v16, v161, v16
	v_max_f32_e32 v161, v163, v164
	v_min_f32_e32 v163, v163, v164
	v_max_f32_e32 v164, v165, v166
	v_min_f32_e32 v165, v165, v166
	v_max_f32_e32 v166, v162, v25
	v_min_f32_e32 v25, v162, v25
	v_max_f32_e32 v162, v167, v29
	v_min_f32_e32 v29, v167, v29
	v_max_f32_e32 v167, v31, v143
	v_min_f32_e32 v31, v31, v143
	v_max_f32_e32 v143, v27, v30
	v_min_f32_e32 v27, v27, v30
	v_max_f32_e32 v30, v26, v28
	v_min_f32_e32 v26, v26, v28
	v_max_f32_e32 v28, v145, v149
	v_min_f32_e32 v145, v145, v149
	v_max_f32_e32 v149, v147, v146
	v_min_f32_e32 v146, v147, v146
	v_max_f32_e32 v147, v144, v148
	v_min_f32_e32 v144, v144, v148
	v_max_f32_e32 v148, v150, v151
	v_min_f32_e32 v150, v150, v151
	v_max_f32_e32 v151, v152, v156
	v_min_f32_e32 v152, v152, v156
	v_max_f32_e32 v156, v158, v159
	v_min_f32_e32 v158, v158, v159
	v_max_f32_e32 v159, v153, v157
	v_min_f32_e32 v153, v153, v157
	v_max_f32_e32 v157, v155, v154
	v_min_f32_e32 v154, v155, v154
	v_max_f32_e32 v155, v16, v165
	v_min_f32_e32 v16, v16, v165
	v_max_f32_e32 v165, v163, v25
	v_min_f32_e32 v25, v163, v25
	v_max_f32_e32 v163, v160, v164
	v_min_f32_e32 v160, v160, v164
	v_max_f32_e32 v164, v161, v166
	v_min_f32_e32 v161, v161, v166
	v_max_f32_e32 v166, v162, v167
	v_min_f32_e32 v162, v162, v167
	v_max_f32_e32 v167, v29, v31
	v_min_f32_e32 v29, v29, v31
	v_max_f32_e32 v31, v143, v30
	v_min_f32_e32 v30, v143, v30
	v_max_f32_e32 v143, v27, v26
	v_min_f32_e32 v26, v27, v26
	v_max_f32_e32 v27, v145, v146
	v_min_f32_e32 v145, v145, v146
	v_max_f32_e32 v146, v28, v149
	v_min_f32_e32 v28, v28, v149
	v_max_f32_e32 v149, v144, v150
	v_min_f32_e32 v144, v144, v150
	v_max_f32_e32 v150, v147, v148
	v_min_f32_e32 v147, v147, v148
	v_max_f32_e32 v148, v151, v156
	v_min_f32_e32 v151, v151, v156
	v_max_f32_e32 v156, v152, v158
	v_min_f32_e32 v152, v152, v158
	v_max_f32_e32 v158, v159, v157
	v_min_f32_e32 v157, v159, v157
	v_max_f32_e32 v159, v153, v154
	v_min_f32_e32 v153, v153, v154
	v_max_f32_e32 v154, v16, v25
	v_min_f32_e32 v16, v16, v25
	v_max_f32_e32 v25, v155, v165
	v_min_f32_e32 v155, v155, v165
	v_max_f32_e32 v165, v160, v161
	v_min_f32_e32 v160, v160, v161
	v_max_f32_e32 v161, v163, v164
	v_min_f32_e32 v163, v163, v164
	v_max_f32_e32 v164, v166, v145
	v_min_f32_e32 v145, v166, v145
	v_max_f32_e32 v166, v162, v27
	v_min_f32_e32 v27, v162, v27
	v_max_f32_e32 v162, v167, v28
	v_min_f32_e32 v28, v167, v28
	v_max_f32_e32 v167, v29, v146
	v_min_f32_e32 v29, v29, v146
	v_max_f32_e32 v146, v31, v144
	v_min_f32_e32 v31, v31, v144
	v_max_f32_e32 v144, v30, v149
	v_min_f32_e32 v30, v30, v149
	v_max_f32_e32 v149, v143, v147
	v_min_f32_e32 v143, v143, v147
	v_max_f32_e32 v147, v26, v150
	v_min_f32_e32 v26, v26, v150
	v_max_f32_e32 v150, v148, v16
	v_min_f32_e32 v16, v148, v16
	v_max_f32_e32 v148, v151, v154
	v_min_f32_e32 v151, v151, v154
	v_max_f32_e32 v154, v156, v155
	v_min_f32_e32 v155, v156, v155
	v_max_f32_e32 v156, v152, v25
	v_min_f32_e32 v25, v152, v25
	v_max_f32_e32 v152, v158, v160
	v_min_f32_e32 v158, v158, v160
; template <int N> __device__ __forceinline__ void sortdesc(float (&v)[N]) {
; #pragma unroll
;     for (int k = 2; k <= N; k <<= 1)
; #pragma unroll
;         for (int j = k >> 1; j > 0; j >>= 1)
; #pragma unroll
;             for (int i = 0; i < N; ++i) { const int p = i ^ j;
;                 if (p > i) { const bool desc = ((i & k) == 0); const float a = v[i], b = v[p], hi = fmaxf(a, b), lo = fminf(a, b); v[i] = desc ? hi : lo; v[p] = desc ? lo : hi; } }
; }
; __device__ __forceinline__ void merge16(float (&v)[16]) {
; #pragma unroll
;     for (int j = 8; j > 0; j >>= 1)
; #pragma unroll
;         for (int i = 0; i < 16; ++i) { const int p = i ^ j; if (p > i) { const float a = v[i], b = v[p]; v[i] = fmaxf(a, b); v[p] = fminf(a, b); } }
; }
; __device__ __forceinline__ void top16_of_group(float (&a)[16]) {
; #pragma unroll
;     for (int sh = 16; sh <= 32; sh <<= 1) {
;         float cc[16];
; #pragma unroll
;         for (int i = 0; i < 16; ++i) cc[i] = fmaxf(a[i], __shfl_xor(a[15 - i], sh));
;         merge16(cc);
; #pragma unroll
;         for (int i = 0; i < 16; ++i) a[i] = cc[i];
;     }
; }
	v_max_f32_e32 v160, v157, v165
	v_min_f32_e32 v157, v157, v165
	v_max_f32_e32 v165, v159, v163
	v_min_f32_e32 v159, v159, v163
	v_max_f32_e32 v163, v153, v161
	v_min_f32_e32 v153, v153, v161
	v_max_f32_e32 v161, v164, v146
	v_min_f32_e32 v146, v164, v146
	v_max_f32_e32 v164, v166, v144
	v_min_f32_e32 v144, v166, v144
	v_max_f32_e32 v166, v162, v149
	v_min_f32_e32 v149, v162, v149
	v_max_f32_e32 v162, v167, v147
	v_min_f32_e32 v147, v167, v147
	v_max_f32_e32 v167, v145, v31
	v_min_f32_e32 v31, v145, v31
	v_max_f32_e32 v145, v27, v30
	v_min_f32_e32 v27, v27, v30
	v_max_f32_e32 v30, v28, v143
	v_min_f32_e32 v28, v28, v143
	v_max_f32_e32 v143, v29, v26
	v_min_f32_e32 v26, v29, v26
	v_max_f32_e32 v29, v16, v158
	v_min_f32_e32 v16, v16, v158
	v_max_f32_e32 v158, v151, v157
	v_min_f32_e32 v151, v151, v157
	v_max_f32_e32 v157, v155, v159
	v_min_f32_e32 v155, v155, v159
	v_max_f32_e32 v159, v25, v153
	v_min_f32_e32 v25, v25, v153
	v_max_f32_e32 v153, v150, v152
	v_min_f32_e32 v150, v150, v152
	v_max_f32_e32 v152, v148, v160
	v_min_f32_e32 v148, v148, v160
	v_max_f32_e32 v160, v154, v165
	v_min_f32_e32 v154, v154, v165
	v_max_f32_e32 v165, v156, v163
	v_min_f32_e32 v156, v156, v163
	v_max_f32_e32 v163, v161, v166
	v_min_f32_e32 v161, v161, v166
	v_max_f32_e32 v166, v164, v162
	v_min_f32_e32 v162, v164, v162
	v_max_f32_e32 v164, v146, v149
	v_min_f32_e32 v146, v146, v149
	v_max_f32_e32 v149, v144, v147
	v_min_f32_e32 v144, v144, v147
	v_max_f32_e32 v147, v167, v30
	v_min_f32_e32 v30, v167, v30
	v_max_f32_e32 v167, v145, v143
	v_min_f32_e32 v143, v145, v143
	v_max_f32_e32 v145, v31, v28
	v_min_f32_e32 v28, v31, v28
	v_max_f32_e32 v31, v27, v26
	v_min_f32_e32 v26, v27, v26
	v_max_f32_e32 v27, v16, v155
	v_min_f32_e32 v16, v16, v155
	v_max_f32_e32 v155, v151, v25
	v_min_f32_e32 v25, v151, v25
	v_max_f32_e32 v151, v29, v157
	v_min_f32_e32 v29, v29, v157
	v_max_f32_e32 v157, v158, v159
	v_min_f32_e32 v158, v158, v159
	v_max_f32_e32 v159, v150, v154
	v_min_f32_e32 v150, v150, v154
	v_max_f32_e32 v154, v148, v156
	v_min_f32_e32 v148, v148, v156
	v_max_f32_e32 v156, v153, v160
	v_min_f32_e32 v153, v153, v160
	v_max_f32_e32 v160, v152, v165
	v_min_f32_e32 v152, v152, v165
	v_min_f32_e32 v165, v163, v166
	v_min_f32_e32 v168, v161, v162
	v_min_f32_e32 v169, v164, v149
	v_min_f32_e32 v170, v146, v144
	v_min_f32_e32 v171, v147, v167
	v_min_f32_e32 v172, v30, v143
	v_min_f32_e32 v173, v145, v31
	v_min_f32_e32 v174, v28, v26
	v_min_f32_e32 v175, v16, v25
	v_min_f32_e32 v176, v27, v155
	v_min_f32_e32 v177, v29, v158
	v_min_f32_e32 v178, v151, v157
	v_min_f32_e32 v179, v150, v148
	v_min_f32_e32 v180, v159, v154
	v_min_f32_e32 v181, v153, v152
	v_min_f32_e32 v182, v156, v160
	v_max3_f32 v163, v163, v166, v175
	v_max3_f32 v16, v165, v16, v25
	v_max3_f32 v25, v161, v162, v176
	v_max3_f32 v27, v168, v27, v155
	v_max3_f32 v149, v164, v149, v177
	v_max3_f32 v29, v169, v29, v158
	v_max3_f32 v144, v146, v144, v178
	v_max3_f32 v146, v170, v151, v157
	v_max3_f32 v147, v147, v167, v179
	v_max3_f32 v148, v171, v150, v148
	v_max3_f32 v30, v30, v143, v180
	v_max3_f32 v143, v172, v159, v154
	v_max3_f32 v31, v145, v31, v181
	v_max3_f32 v145, v173, v153, v152
	v_max3_f32 v26, v28, v26, v182
	v_max3_f32 v28, v174, v156, v160
	v_max_f32_e32 v150, v163, v147
	v_min_f32_e32 v147, v163, v147
	v_max_f32_e32 v151, v16, v148
	v_min_f32_e32 v16, v16, v148
	v_max_f32_e32 v148, v25, v30
	v_min_f32_e32 v25, v25, v30
	v_max_f32_e32 v30, v27, v143
	v_min_f32_e32 v27, v27, v143
	v_max_f32_e32 v143, v149, v31
	v_min_f32_e32 v31, v149, v31
	v_max_f32_e32 v149, v29, v145
	v_min_f32_e32 v29, v29, v145
	v_max_f32_e32 v145, v144, v26
	v_min_f32_e32 v26, v144, v26
	v_max_f32_e32 v144, v146, v28
	v_min_f32_e32 v28, v146, v28
	v_max_f32_e32 v146, v150, v143
	v_min_f32_e32 v143, v150, v143
	v_max_f32_e32 v150, v151, v149
	v_min_f32_e32 v149, v151, v149
	v_max_f32_e32 v151, v148, v145
	v_min_f32_e32 v145, v148, v145
	v_max_f32_e32 v148, v30, v144
	v_min_f32_e32 v30, v30, v144
	v_max_f32_e32 v144, v147, v31
	v_min_f32_e32 v31, v147, v31
	v_max_f32_e32 v147, v16, v29
	v_min_f32_e32 v16, v16, v29
	v_max_f32_e32 v29, v25, v26
	v_min_f32_e32 v25, v25, v26
	v_max_f32_e32 v26, v27, v28
	v_min_f32_e32 v27, v27, v28
	v_max_f32_e32 v28, v146, v151
	v_min_f32_e32 v146, v146, v151
	v_max_f32_e32 v151, v150, v148
	v_min_f32_e32 v148, v150, v148
	v_max_f32_e32 v150, v143, v145
	v_min_f32_e32 v143, v143, v145
	v_max_f32_e32 v145, v149, v30
	v_min_f32_e32 v30, v149, v30
	v_max_f32_e32 v149, v144, v29
	v_min_f32_e32 v29, v144, v29
	v_max_f32_e32 v144, v147, v26
	v_min_f32_e32 v26, v147, v26
	v_max_f32_e32 v147, v31, v25
	v_min_f32_e32 v25, v31, v25
	v_max_f32_e32 v31, v16, v27
	v_min_f32_e32 v16, v16, v27
	v_max_f32_e32 v27, v28, v151
	v_min_f32_e32 v28, v28, v151
	v_max_f32_e32 v151, v146, v148
	v_min_f32_e32 v146, v146, v148
	v_max_f32_e32 v148, v150, v145
	v_min_f32_e32 v145, v150, v145
	v_max_f32_e32 v150, v143, v30
	v_min_f32_e32 v30, v143, v30
	v_max_f32_e32 v143, v149, v144
	ds_bpermute_b32 v158, v70, v143
	v_min_f32_e32 v144, v149, v144
	v_max_f32_e32 v149, v29, v26
	ds_bpermute_b32 v156, v70, v149
	ds_bpermute_b32 v157, v70, v144
	s_waitcnt lgkmcnt(2)
	v_max_f32_e32 v158, v158, v158
	v_max_f32_e32 v158, v30, v158
	ds_bpermute_b32 v30, v70, v30
	s_waitcnt lgkmcnt(2)
	v_max_f32_e32 v156, v156, v156
	v_max_f32_e32 v156, v145, v156
	v_min_f32_e32 v26, v29, v26
	v_max_f32_e32 v29, v147, v31
	s_waitcnt lgkmcnt(0)
	v_max_f32_e32 v30, v30, v30
	v_max_f32_e32 v30, v143, v30
	ds_bpermute_b32 v143, v70, v150
	v_min_f32_e32 v31, v147, v31
	v_max_f32_e32 v147, v25, v16
	v_min_f32_e32 v16, v25, v16
	ds_bpermute_b32 v25, v70, v16
	s_waitcnt lgkmcnt(1)
; #define GAS __attribute__((address_space(1)))
; #define LAS __attribute__((address_space(3)))
; __device__ __forceinline__ void top16_of_group(float (&a)[16]) {
; #pragma unroll
;     for (int sh = 16; sh <= 32; sh <<= 1) {
;         float cc[16];
; #pragma unroll
;         for (int i = 0; i < 16; ++i) cc[i] = fmaxf(a[i], __shfl_xor(a[15 - i], sh));
;         merge16(cc);
; #pragma unroll
;         for (int i = 0; i < 16; ++i) a[i] = cc[i];
;     }
; }
; __device__ __forceinline__ void topk_task(const Frame& F, int l, int tb, int h, const LAS unsigned char* kl, LAS float* tl, const LAS unsigned char* cab) {
;     int lane = lane_id(); asm volatile("" : "+v"(lane));
;     const int c = lane & 15, rq = lane >> 4;
;     const int t0 = tb * 16;
;     const bf16* QP = (const bf16*)(F.ws + WS_QP);
;     int* EXPI = (int*)(F.ws + WS_EXP); float* GATE = (float*)(F.ws + WS_GATE);
;     const float NEG = -__builtin_inff();
;     bf16x8 Qall[2][4];
; #pragma unroll
;     for (int p = 0; p < 2; ++p)
; #pragma unroll
;         for (int ks = 0; ks < 4; ++ks) Qall[p][ks] = ld_b8(QP + (size_t)(t0 + c) * QPP + h * 256 + p * 128 + ks * 32 + rq * 8);
;     float rsp[8];
;     { const float* SS2 = (const float*)(F.ws + WS_SS2) + (t0 + c);
; #pragma unroll
;         for (int i = 0; i < 8; ++i) rsp[i] = *(const GAS float*)(SS2 + (size_t)(rq * 8 + i) * T); }
; #pragma unroll
;     for (int p = 0; p < 2; ++p) {
;         bf16x8 Qf[4];
; #pragma unroll
;         for (int ks = 0; ks < 4; ++ks) Qf[ks] = Qall[p][ks];
;         float v[32];
;         const LAS unsigned char* kbase = kl + (p * 128 + c) * KL_PITCH + rq * 16;
; #pragma unroll
;         for (int kb = 0; kb < 8; ++kb) {
;             f32x4 a = (f32x4){0.f, 0.f, 0.f, 0.f};
; #pragma unroll
;             for (int ks = 0; ks < 4; ++ks) a = mfma16(*(const LAS bf16x8*)(kbase + kb * 16 * KL_PITCH + ks * 64), Qf[ks], a);
; #pragma unroll
;             for (int e = 0; e < 4; ++e) v[kb * 4 + e] = embed_idx<127u>(a[e], (unsigned)(kb * 16 + rq * 4 + e));
;         }
;         sortdesc<32>(v);
;         float top[16];
; #pragma unroll
;         for (int i = 0; i < 16; ++i) top[i] = v[i];
;         top16_of_group(top);
;         if (rq == 0) {
; #pragma unroll
;             for (int it = 0; it < 16; ++it) tl[(p * 16 + c) * TL_STRIDE + it] = top[it];
	v_max_f32_e32 v143, v143, v143
	v_max_f32_e32 v143, v144, v143
	ds_bpermute_b32 v144, v70, v145
	ds_bpermute_b32 v145, v70, v148
	ds_bpermute_b32 v152, v70, v147
	ds_bpermute_b32 v155, v70, v26
	s_waitcnt lgkmcnt(4)
	v_max_f32_e32 v25, v25, v25
	v_max_f32_e32 v25, v27, v25
	s_waitcnt lgkmcnt(2)
	v_max_f32_e32 v145, v145, v145
	v_max_f32_e32 v26, v26, v145
	ds_bpermute_b32 v145, v70, v146
	s_waitcnt lgkmcnt(2)
	v_max_f32_e32 v152, v152, v152
	v_max_f32_e32 v152, v28, v152
	ds_bpermute_b32 v153, v70, v31
	ds_bpermute_b32 v154, v70, v29
	s_waitcnt lgkmcnt(2)
	v_max_f32_e32 v145, v145, v145
	v_max_f32_e32 v29, v29, v145
	ds_bpermute_b32 v145, v70, v151
	ds_bpermute_b32 v28, v70, v28
	ds_bpermute_b32 v27, v70, v27
	s_waitcnt lgkmcnt(4)
	v_max_f32_e32 v153, v153, v153
	s_waitcnt lgkmcnt(3)
	v_max_f32_e32 v154, v154, v154
	v_max_f32_e32 v155, v155, v155
	v_max_f32_e32 v157, v157, v157
	v_max_f32_e32 v144, v144, v144
	s_waitcnt lgkmcnt(2)
	v_max_f32_e32 v145, v145, v145
	s_waitcnt lgkmcnt(1)
	v_max_f32_e32 v28, v28, v28
	s_waitcnt lgkmcnt(0)
	v_max_f32_e32 v27, v27, v27
	v_max_f32_e32 v153, v151, v153
	v_max_f32_e32 v154, v146, v154
	v_max_f32_e32 v155, v148, v155
	v_max_f32_e32 v157, v150, v157
	v_max_f32_e32 v144, v149, v144
	v_max_f32_e32 v31, v31, v145
	v_max_f32_e32 v28, v147, v28
	v_max_f32_e32 v16, v16, v27
	v_max_f32_e32 v27, v25, v30
	v_min_f32_e32 v25, v25, v30
	v_max_f32_e32 v30, v152, v143
	v_min_f32_e32 v143, v152, v143
	v_max_f32_e32 v145, v153, v144
	v_min_f32_e32 v144, v153, v144
	v_max_f32_e32 v146, v154, v26
	v_min_f32_e32 v26, v154, v26
	v_max_f32_e32 v147, v155, v29
	v_min_f32_e32 v29, v155, v29
	v_max_f32_e32 v148, v156, v31
	v_min_f32_e32 v31, v156, v31
	v_max_f32_e32 v149, v157, v28
	v_min_f32_e32 v28, v157, v28
	v_max_f32_e32 v150, v158, v16
	v_min_f32_e32 v16, v158, v16
	v_max_f32_e32 v151, v27, v147
	v_min_f32_e32 v27, v27, v147
	v_max_f32_e32 v147, v30, v148
	v_min_f32_e32 v30, v30, v148
	v_max_f32_e32 v148, v145, v149
	v_min_f32_e32 v145, v145, v149
	v_max_f32_e32 v149, v146, v150
	v_min_f32_e32 v146, v146, v150
	v_max_f32_e32 v150, v25, v29
	v_min_f32_e32 v25, v25, v29
	v_max_f32_e32 v29, v143, v31
	v_min_f32_e32 v31, v143, v31
	v_max_f32_e32 v143, v144, v28
	v_min_f32_e32 v28, v144, v28
	v_max_f32_e32 v144, v26, v16
	v_min_f32_e32 v16, v26, v16
	v_max_f32_e32 v26, v151, v148
	v_min_f32_e32 v148, v151, v148
	v_max_f32_e32 v151, v147, v149
	v_min_f32_e32 v147, v147, v149
	v_max_f32_e32 v149, v27, v145
	v_min_f32_e32 v27, v27, v145
	v_max_f32_e32 v145, v30, v146
	v_min_f32_e32 v146, v30, v146
	v_max_f32_e32 v152, v150, v143
	v_min_f32_e32 v143, v150, v143
	v_max_f32_e32 v153, v29, v144
	v_min_f32_e32 v144, v29, v144
	v_max_f32_e32 v155, v25, v28
	v_min_f32_e32 v158, v25, v28
	v_max_f32_e32 v160, v31, v16
	v_min_f32_e32 v16, v31, v16
	v_max_f32_e32 v157, v26, v151
	v_min_f32_e32 v30, v26, v151
	v_max_f32_e32 v150, v148, v147
	v_min_f32_e32 v26, v148, v147
	v_max_f32_e32 v156, v149, v145
	v_min_f32_e32 v29, v149, v145
	v_max_f32_e32 v148, v27, v146
	v_min_f32_e32 v25, v27, v146
	v_max_f32_e32 v161, v152, v153
	v_min_f32_e32 v145, v152, v153
	v_max_f32_e32 v154, v143, v144
	v_min_f32_e32 v28, v143, v144
	v_max_f32_e32 v159, v155, v160
	v_min_f32_e32 v143, v155, v160
	v_max_f32_e32 v152, v158, v16
	v_min_f32_e32 v27, v158, v16
	ds_bpermute_b32 v165, v71, v27
	ds_bpermute_b32 v151, v71, v152
	ds_bpermute_b32 v160, v71, v143
	ds_bpermute_b32 v144, v71, v159
	ds_bpermute_b32 v164, v71, v28
	ds_bpermute_b32 v149, v71, v154
	ds_bpermute_b32 v158, v71, v145
	ds_bpermute_b32 v31, v71, v161
	ds_bpermute_b32 v167, v71, v25
	ds_bpermute_b32 v155, v71, v148
	ds_bpermute_b32 v163, v71, v29
	ds_bpermute_b32 v147, v71, v156
	ds_bpermute_b32 v166, v71, v26
	ds_bpermute_b32 v153, v71, v150
	ds_bpermute_b32 v162, v71, v30
	ds_bpermute_b32 v146, v71, v157
	v_mul_lo_u32 v16, v90, s7
	v_add_u32_e32 v16, s73, v16
	s_and_saveexec_b64 s[0:1], s[34:35]
	s_cbranch_execz .LBB0_1011
; #define GAS __attribute__((address_space(1)))
; #define LAS __attribute__((address_space(3)))
; __device__ __forceinline__ f32x4 mfma16(bf16x8 a, bf16x8 b, f32x4 c) { return __builtin_amdgcn_mfma_f32_16x16x32_bf16(a, b, c, 0, 0, 0); }
; __device__ __forceinline__ void top16_of_group(float (&a)[16]) {
;     ...
;         for (int i = 0; i < 16; ++i) cc[i] = fmaxf(a[i], __shfl_xor(a[15 - i], sh));
;         merge16(cc);
; #pragma unroll
;         for (int i = 0; i < 16; ++i) a[i] = cc[i];
;     }
; }
; __device__ __forceinline__ void topk_task(const Frame& F, int l, int tb, int h, const LAS unsigned char* kl, LAS float* tl, const LAS unsigned char* cab) {
;     int lane = lane_id(); asm volatile("" : "+v"(lane));
;     const int c = lane & 15, rq = lane >> 4;
;     const int t0 = tb * 16;
;     const bf16* QP = (const bf16*)(F.ws + WS_QP);
;     int* EXPI = (int*)(F.ws + WS_EXP); float* GATE = (float*)(F.ws + WS_GATE);
;     const float NEG = -__builtin_inff();
;     bf16x8 Qall[2][4];
; #pragma unroll
;     for (int p = 0; p < 2; ++p)
; #pragma unroll
;         for (int ks = 0; ks < 4; ++ks) Qall[p][ks] = ld_b8(QP + (size_t)(t0 + c) * QPP + h * 256 + p * 128 + ks * 32 + rq * 8);
;     float rsp[8];
;     { const float* SS2 = (const float*)(F.ws + WS_SS2) + (t0 + c);
; #pragma unroll
;         for (int i = 0; i < 8; ++i) rsp[i] = *(const GAS float*)(SS2 + (size_t)(rq * 8 + i) * T); }
; #pragma unroll
;     for (int p = 0; p < 2; ++p) {
;         bf16x8 Qf[4];
; #pragma unroll
;         for (int ks = 0; ks < 4; ++ks) Qf[ks] = Qall[p][ks];
;         float v[32];
;         const LAS unsigned char* kbase = kl + (p * 128 + c) * KL_PITCH + rq * 16;
; #pragma unroll
;         for (int kb = 0; kb < 8; ++kb) {
;             f32x4 a = (f32x4){0.f, 0.f, 0.f, 0.f};
; #pragma unroll
;             for (int ks = 0; ks < 4; ++ks) a = mfma16(*(const LAS bf16x8*)(kbase + kb * 16 * KL_PITCH + ks * 64), Qf[ks], a);
; #pragma unroll
;             for (int e = 0; e < 4; ++e) v[kb * 4 + e] = embed_idx<127u>(a[e], (unsigned)(kb * 16 + rq * 4 + e));
;         }
;         sortdesc<32>(v);
;         float top[16];
; #pragma unroll
;         for (int i = 0; i < 16; ++i) top[i] = v[i];
;         top16_of_group(top);
;         if (rq == 0) {
; #pragma unroll
;             for (int it = 0; it < 16; ++it) tl[(p * 16 + c) * TL_STRIDE + it] = top[it];
;         }
	s_waitcnt lgkmcnt(14)
	v_max_f32_e32 v90, v165, v165
	v_max_f32_e32 v157, v157, v157
	s_waitcnt lgkmcnt(11)
	v_max_f32_e32 v164, v164, v164
	v_max_f32_e32 v156, v156, v156
	v_max_f32_e32 v160, v160, v160
	v_max_f32_e32 v150, v150, v150
	s_waitcnt lgkmcnt(9)
	v_max_f32_e32 v158, v158, v158
	v_max_f32_e32 v148, v148, v148
	v_max_f32_e32 v151, v151, v151
	v_max_f32_e32 v30, v30, v30
	v_max_f32_e32 v149, v149, v149
	v_max_f32_e32 v29, v29, v29
	v_max_f32_e32 v144, v144, v144
	v_max_f32_e32 v26, v26, v26
	s_waitcnt lgkmcnt(8)
	v_max_f32_e32 v31, v31, v31
	v_max_f32_e32 v25, v25, v25
	v_max_f32_e32 v90, v157, v90
	s_waitcnt lgkmcnt(7)
	v_max_f32_e32 v157, v167, v167
	v_max_f32_e32 v161, v161, v161
	v_max_f32_e32 v156, v156, v164
	s_waitcnt lgkmcnt(3)
	v_max_f32_e32 v164, v166, v166
	v_max_f32_e32 v159, v159, v159
	v_max_f32_e32 v150, v150, v160
	v_max_f32_e32 v160, v163, v163
	v_max_f32_e32 v154, v154, v154
	v_max_f32_e32 v148, v148, v158
	s_waitcnt lgkmcnt(1)
	v_max_f32_e32 v158, v162, v162
	v_max_f32_e32 v152, v152, v152
	v_max_f32_e32 v30, v30, v151
	v_max_f32_e32 v151, v155, v155
	v_max_f32_e32 v145, v145, v145
	v_max_f32_e32 v29, v29, v149
	v_max_f32_e32 v149, v153, v153
	v_max_f32_e32 v143, v143, v143
	v_max_f32_e32 v26, v26, v144
	v_max_f32_e32 v144, v147, v147
	v_max_f32_e32 v28, v28, v28
	v_max_f32_e32 v25, v25, v31
	s_waitcnt lgkmcnt(0)
	v_max_f32_e32 v31, v146, v146
	v_max_f32_e32 v27, v27, v27
	v_max_f32_e32 v157, v161, v157
	v_max_f32_e32 v159, v159, v164
	v_max_f32_e32 v154, v154, v160
	v_max_f32_e32 v152, v152, v158
	v_max_f32_e32 v145, v145, v151
	v_max_f32_e32 v143, v143, v149
	v_max_f32_e32 v28, v28, v144
	v_max_f32_e32 v27, v27, v31
	v_min_f32_e32 v161, v90, v157
	v_min_f32_e32 v164, v156, v159
	v_min_f32_e32 v160, v150, v154
	v_min_f32_e32 v158, v148, v152
	v_min_f32_e32 v151, v30, v145
	v_min_f32_e32 v149, v29, v143
	v_min_f32_e32 v144, v26, v28
	v_min_f32_e32 v31, v25, v27
	v_max_f32_e32 v90, v90, v157
	v_max_f32_e32 v156, v156, v159
	v_max_f32_e32 v150, v150, v154
	v_max_f32_e32 v148, v148, v152
	v_max_f32_e32 v30, v30, v145
	v_max_f32_e32 v29, v29, v143
	v_max_f32_e32 v26, v26, v28
	v_max_f32_e32 v25, v25, v27
	v_min_f32_e32 v157, v90, v156
	v_min_f32_e32 v152, v150, v148
	v_min_f32_e32 v143, v30, v29
	v_min_f32_e32 v27, v26, v25
	v_max_f32_e32 v90, v90, v156
	v_max_f32_e32 v148, v150, v148
	v_max_f32_e32 v29, v30, v29
	v_max_f32_e32 v25, v26, v25
	v_min_f32_e32 v165, v161, v164
	v_min_f32_e32 v162, v160, v158
	v_min_f32_e32 v153, v151, v149
	v_min_f32_e32 v146, v144, v31
	v_max_f32_e32 v161, v161, v164
	v_max_f32_e32 v158, v160, v158
	v_max_f32_e32 v149, v151, v149
	v_max_f32_e32 v31, v144, v31
	v_min_f32_e32 v150, v90, v148
	v_min_f32_e32 v26, v29, v25
	v_max_f32_e32 v90, v90, v148
	v_max_f32_e32 v25, v29, v25
	v_min_f32_e32 v163, v165, v162
	v_min_f32_e32 v147, v153, v146
	v_max_f32_e32 v162, v165, v162
	v_max_f32_e32 v146, v153, v146
	v_min_f32_e32 v160, v161, v158
	v_min_f32_e32 v144, v149, v31
	v_max_f32_e32 v158, v161, v158
	v_max_f32_e32 v31, v149, v31
	v_min_f32_e32 v154, v157, v152
	v_min_f32_e32 v28, v143, v27
	v_max_f32_e32 v152, v157, v152
	v_max_f32_e32 v27, v143, v27
	v_min_f32_e32 v29, v90, v25
	v_max_f32_e32 v25, v90, v25
	v_min_f32_e32 v155, v163, v147
	v_max_f32_e32 v147, v163, v147
	v_min_f32_e32 v153, v162, v146
	v_max_f32_e32 v146, v162, v146
	v_min_f32_e32 v151, v160, v144
	v_max_f32_e32 v144, v160, v144
	v_min_f32_e32 v149, v158, v31
	v_max_f32_e32 v31, v158, v31
	v_min_f32_e32 v145, v154, v28
	v_max_f32_e32 v28, v154, v28
	v_min_f32_e32 v143, v152, v27
	v_max_f32_e32 v27, v152, v27
	v_min_f32_e32 v30, v150, v26
	v_max_f32_e32 v26, v150, v26
	ds_write2_b32 v16, v25, v29 offset1:1
	ds_write2_b32 v16, v26, v30 offset0:2 offset1:3
	ds_write2_b32 v16, v27, v143 offset0:4 offset1:5
	ds_write2_b32 v16, v28, v145 offset0:6 offset1:7
	ds_write2_b32 v16, v31, v149 offset0:8 offset1:9
	ds_write2_b32 v16, v144, v151 offset0:10 offset1:11
	ds_write2_b32 v16, v146, v153 offset0:12 offset1:13
	ds_write2_b32 v16, v147, v155 offset0:14 offset1:15
